# v22
# speedup vs baseline: 1.0296x; 1.0296x over previous
_Z12pool1_kernelPKfS0_S0_S0_S0_S0_S0_S0_S0_S0_PfS1_:
	s_load_dwordx4 s[12:15], s[0:1], 0x0
	s_load_dwordx2 s[36:37], s[0:1], 0x48
	s_load_dwordx2 s[38:39], s[0:1], 0x58
	s_load_dwordx2 s[48:49], s[0:1], 0x20
	s_cmp_eq_u32 s2, 0
	s_movk_i32 s3, 0x80
	s_cselect_b64 s[4:5], -1, 0
	v_cmp_gt_u32_e64 s[10:11], s3, v0
	s_and_b64 s[6:7], s[4:5], s[10:11]
	s_and_saveexec_b64 s[4:5], s[6:7]
	s_cbranch_execz .LBB0_2
	v_mov_b32_e32 v1, 0
	v_lshlrev_b64 v[2:3], 2, v[0:1]
	s_waitcnt lgkmcnt(0)
	v_lshl_add_u64 v[4:5], s[36:37], 0, v[2:3]
	global_load_dword v253, v[4:5], off
	v_lshl_add_u64 v[254:255], s[38:39], 0, v[2:3]
.LBB0_2:
	s_or_b64 exec, exec, s[4:5]
	v_mov_b32_e32 v3, 0
	v_lshlrev_b32_e32 v130, 2, v0
	v_and_b32_e32 v131, 63, v0
	v_readfirstlane_b32 s3, v0
	v_lshlrev_b32_e32 v204, 4, v131
	v_lshlrev_b32_e32 v222, 4, v0
	v_add_u32_e32 v223, 0x2000, v222
	v_add_u32_e32 v224, 0x4000, v222
	v_add_u32_e32 v225, 0x6000, v222
	v_add_u32_e32 v226, 0x8000, v222
	v_add_u32_e32 v227, 0xa000, v222
	v_add_u32_e32 v228, 0xc000, v222
	v_add_u32_e32 v229, 0xe000, v222
	v_add_u32_e32 v230, 0x10000, v222
	v_add_u32_e32 v231, 0x12000, v222
	v_add_u32_e32 v232, 0x14000, v222
	v_add_u32_e32 v233, 0x16000, v222
	v_add_u32_e32 v234, 0x18000, v222
	v_add_u32_e32 v235, 0x1a000, v222
	v_add_u32_e32 v236, 0x1c000, v222
	v_add_u32_e32 v237, 0x1e000, v222
	s_lshr_b32 s31, s3, 6
	s_lshl_b32 s33, s2, 21
	s_waitcnt lgkmcnt(0)
	s_mov_b64 s[40:41], s[14:15]
	s_load_dword s43, s[48:49], 0x0
	s_mov_b32 s15, 0x20000
	s_brev_b32 s14, -2
	s_and_b32 s13, s13, 0xffff
	global_load_dwordx4 v[4:7], v222, s[40:41]
	global_load_dwordx4 v[8:11], v223, s[40:41]
	global_load_dwordx4 v[12:15], v224, s[40:41]
	global_load_dwordx4 v[16:19], v225, s[40:41]
	global_load_dwordx4 v[20:23], v226, s[40:41]
	global_load_dwordx4 v[24:27], v227, s[40:41]
	global_load_dwordx4 v[28:31], v228, s[40:41]
	global_load_dwordx4 v[98:101], v229, s[40:41]
	global_load_dwordx4 v[102:105], v230, s[40:41]
	global_load_dwordx4 v[106:109], v231, s[40:41]
	global_load_dwordx4 v[110:113], v232, s[40:41]
	global_load_dwordx4 v[114:117], v233, s[40:41]
	global_load_dwordx4 v[118:121], v234, s[40:41]
	global_load_dwordx4 v[122:125], v235, s[40:41]
	global_load_dwordx4 v[126:129], v236, s[40:41]
	global_load_dwordx4 v[132:135], v237, s[40:41]
	s_load_dwordx2 s[20:21], s[0:1], 0x50
	s_load_dwordx2 s[22:23], s[0:1], 0x40
	s_load_dwordx2 s[4:5], s[0:1], 0x20
	s_load_dwordx4 s[16:19], s[0:1], 0x30
	s_lshl_b32 s6, s31, 14
	s_add_i32 s6, s6, s33
	s_or_b32 s7, s6, 0x1000
	buffer_load_dwordx4 v[34:37], v204, s[12:15], s6 offen sc0 nt sc1
	buffer_load_dwordx4 v[38:41], v204, s[12:15], s7 offen sc0 nt sc1
	s_or_b32 s7, s6, 0x2000
	s_or_b32 s8, s6, 0x3000
	buffer_load_dwordx4 v[42:45], v204, s[12:15], s7 offen sc0 nt sc1
	buffer_load_dwordx4 v[46:49], v204, s[12:15], s8 offen sc0 nt sc1
	s_or_b32 s7, s6, 0x400
	s_or_b32 s8, s6, 0x1400
	buffer_load_dwordx4 v[50:53], v204, s[12:15], s7 offen sc0 nt sc1
	buffer_load_dwordx4 v[54:57], v204, s[12:15], s8 offen sc0 nt sc1
	s_or_b32 s7, s6, 0x2400
	s_or_b32 s8, s6, 0x3400
	buffer_load_dwordx4 v[58:61], v204, s[12:15], s7 offen sc0 nt sc1
	buffer_load_dwordx4 v[62:65], v204, s[12:15], s8 offen sc0 nt sc1
	s_or_b32 s7, s6, 0x800
	s_or_b32 s8, s6, 0x1800
	buffer_load_dwordx4 v[66:69], v204, s[12:15], s7 offen sc0 nt sc1
	buffer_load_dwordx4 v[70:73], v204, s[12:15], s8 offen sc0 nt sc1
	s_or_b32 s7, s6, 0x2800
	s_or_b32 s8, s6, 0x3800
	buffer_load_dwordx4 v[74:77], v204, s[12:15], s7 offen sc0 nt sc1
	buffer_load_dwordx4 v[78:81], v204, s[12:15], s8 offen sc0 nt sc1
	s_or_b32 s7, s6, 0xc00
	s_or_b32 s8, s6, 0x1c00
	buffer_load_dwordx4 v[82:85], v204, s[12:15], s7 offen sc0 nt sc1
	buffer_load_dwordx4 v[86:89], v204, s[12:15], s8 offen sc0 nt sc1
	s_or_b32 s7, s6, 0x2c00
	s_or_b32 s6, s6, 0x3c00
	buffer_load_dwordx4 v[90:93], v204, s[12:15], s7 offen sc0 nt sc1
	buffer_load_dwordx4 v[94:97], v204, s[12:15], s6 offen sc0 nt sc1
	v_lshlrev_b32_e32 v2, 3, v0
	v_and_b32_e32 v1, 0x1f8, v2
	v_lshrrev_b32_e32 v32, 6, v0
	s_movk_i32 s6, 0x220
	s_waitcnt vmcnt(31)
	v_cvt_pk_bf16_f32 v4, v4, v5
	v_cvt_pk_bf16_f32 v5, v6, v7
	v_mad_u32_u24 v6, v32, s6, v1
	ds_write_b64 v6, v[4:5]
	v_add_u32_e32 v4, 0x200, v0
	v_lshrrev_b32_e32 v7, 6, v4
	s_waitcnt vmcnt(30)
	v_cvt_pk_bf16_f32 v4, v8, v9
	v_cvt_pk_bf16_f32 v5, v10, v11
	v_mad_u32_u24 v7, v7, s6, v1
	ds_write_b64 v7, v[4:5]
	s_waitcnt vmcnt(29)
	v_cvt_pk_bf16_f32 v4, v12, v13
	v_cvt_pk_bf16_f32 v5, v14, v15
	ds_write_b64 v6, v[4:5] offset:8704
	v_add_u32_e32 v4, 0x600, v0
	v_lshrrev_b32_e32 v7, 6, v4
	s_waitcnt vmcnt(28)
	v_cvt_pk_bf16_f32 v4, v16, v17
	v_cvt_pk_bf16_f32 v5, v18, v19
	v_mad_u32_u24 v7, v7, s6, v1
	ds_write_b64 v7, v[4:5]
	s_waitcnt vmcnt(27)
	v_cvt_pk_bf16_f32 v4, v20, v21
	v_cvt_pk_bf16_f32 v5, v22, v23
	ds_write_b64 v6, v[4:5] offset:17408
	v_add_u32_e32 v4, 0xa00, v0
	v_lshrrev_b32_e32 v7, 6, v4
	s_waitcnt vmcnt(26)
	v_cvt_pk_bf16_f32 v4, v24, v25
	v_cvt_pk_bf16_f32 v5, v26, v27
	v_mad_u32_u24 v7, v7, s6, v1
	ds_write_b64 v7, v[4:5]
	s_waitcnt vmcnt(25)
	v_cvt_pk_bf16_f32 v4, v28, v29
	v_cvt_pk_bf16_f32 v5, v30, v31
	ds_write_b64 v6, v[4:5] offset:26112
	v_add_u32_e32 v4, 0xe00, v0
	v_lshrrev_b32_e32 v7, 6, v4
	s_waitcnt vmcnt(24)
	v_cvt_pk_bf16_f32 v4, v98, v99
	v_cvt_pk_bf16_f32 v5, v100, v101
	v_mad_u32_u24 v7, v7, s6, v1
	ds_write_b64 v7, v[4:5]
	s_waitcnt vmcnt(23)
	v_cvt_pk_bf16_f32 v4, v102, v103
	v_cvt_pk_bf16_f32 v5, v104, v105
	ds_write_b64 v6, v[4:5] offset:34816
	v_add_u32_e32 v4, 0x1200, v0
	v_lshrrev_b32_e32 v7, 6, v4
	s_waitcnt vmcnt(22)
	v_cvt_pk_bf16_f32 v4, v106, v107
	v_cvt_pk_bf16_f32 v5, v108, v109
	v_mad_u32_u24 v7, v7, s6, v1
	ds_write_b64 v7, v[4:5]
	s_waitcnt vmcnt(21)
	v_cvt_pk_bf16_f32 v4, v110, v111
	v_cvt_pk_bf16_f32 v5, v112, v113
	ds_write_b64 v6, v[4:5] offset:43520
	v_add_u32_e32 v4, 0x1600, v0
	v_lshrrev_b32_e32 v7, 6, v4
	s_waitcnt vmcnt(20)
	v_cvt_pk_bf16_f32 v4, v114, v115
	v_cvt_pk_bf16_f32 v5, v116, v117
	v_mad_u32_u24 v7, v7, s6, v1
	ds_write_b64 v7, v[4:5]
	s_waitcnt vmcnt(19)
	v_cvt_pk_bf16_f32 v4, v118, v119
	v_cvt_pk_bf16_f32 v5, v120, v121
	ds_write_b64 v6, v[4:5] offset:52224
	v_add_u32_e32 v4, 0x1a00, v0
	v_lshrrev_b32_e32 v7, 6, v4
	s_waitcnt vmcnt(18)
	v_cvt_pk_bf16_f32 v4, v122, v123
	v_cvt_pk_bf16_f32 v5, v124, v125
	v_mad_u32_u24 v7, v7, s6, v1
	ds_write_b64 v7, v[4:5]
	s_waitcnt vmcnt(17)
	v_cvt_pk_bf16_f32 v4, v126, v127
	v_cvt_pk_bf16_f32 v5, v128, v129
	ds_write_b64 v6, v[4:5] offset:60928
	v_add_u32_e32 v4, 0x1e00, v0
	v_lshrrev_b32_e32 v6, 6, v4
	s_waitcnt vmcnt(16)
	v_cvt_pk_bf16_f32 v4, v132, v133
	v_cvt_pk_bf16_f32 v5, v134, v135
	v_mad_u32_u24 v1, v6, s6, v1
	ds_write_b64 v1, v[4:5]
	s_and_saveexec_b64 s[6:7], s[10:11]
	s_cbranch_execz .LBB0_4
	s_load_dwordx4 s[24:27], s[0:1], 0x10
	v_mov_b32_e32 v1, v3
	v_lshlrev_b64 v[4:5], 2, v[0:1]
	s_waitcnt lgkmcnt(0)
	v_lshl_add_u64 v[6:7], s[24:25], 0, v[4:5]
	global_load_dword v1, v[6:7], off
	v_lshl_add_u64 v[4:5], s[26:27], 0, v[4:5]
	global_load_dword v4, v[4:5], off
	v_add_u32_e32 v5, 0x22000, v130
	v_add_u32_e32 v6, 0x22200, v130
	s_waitcnt vmcnt(1)
	v_mul_f32_e32 v1, 0x4038aa3b, v1
	ds_write_b32 v5, v1
	s_waitcnt vmcnt(0)
	ds_write_b32 v6, v4

.LBB0_5:
	v_mad_legacy_u16 v2, v6, s8, v4
	v_lshlrev_b16_e32 v8, 15, v2
	v_lshrrev_b16_e32 v2, 1, v2
	v_cmp_lt_u32_e32 vcc, s24, v6
	v_or_b32_e32 v2, v2, v8
	s_or_b64 s[0:1], vcc, s[0:1]
	v_cmp_gt_u16_e32 vcc, s9, v2
	v_add_u32_e32 v7, 0x200, v6
	v_mov_b32_e32 v6, v7
	v_cndmask_b32_e32 v2, 0, v5, vcc
	ds_write_b64 v1, v[2:3]
	v_add_u32_e32 v1, 0x1000, v1
	s_andn2_b64 exec, exec, s[0:1]
	s_cbranch_execnz .LBB0_5
	s_or_b64 exec, exec, s[0:1]
	s_mov_b32 s34, 0
	v_cmp_eq_u32_e64 s[0:1], 0, v0
	s_and_saveexec_b64 s[8:9], s[0:1]
	v_mov_b32_e32 v1, 8
	v_mov_b32_e32 v2, 0x23420
	ds_write_b32 v2, v1
	s_or_b64 exec, exec, s[8:9]
	v_lshlrev_b32_e32 v1, 2, v131
	v_or_b32_e32 v2, 0x22200, v1
	v_or_b32_e32 v3, 0x22300, v1
	s_waitcnt lgkmcnt(0)
	s_barrier
	ds_read_b32 v2, v2
	ds_read_b32 v3, v3
	v_and_b32_e32 v202, 15, v0
	s_lshl_b32 s30, s31, 4
	v_or_b32_e32 v132, s30, v202
	s_waitcnt lgkmcnt(0)
	v_add_f32_e32 v2, v2, v3
	v_mbcnt_lo_u32_b32 v3, -1, 0
	v_mbcnt_hi_u32_b32 v3, -1, v3
	v_and_b32_e32 v4, 64, v3
	v_add_u32_e32 v4, 64, v4
	v_xor_b32_e32 v5, 32, v3
	v_cmp_lt_i32_e32 vcc, v5, v4
	v_mov_b32_e32 v133, 0
	v_lshrrev_b32_e32 v209, 4, v131
	v_cndmask_b32_e32 v5, v3, v5, vcc
	v_lshlrev_b32_e32 v200, 2, v5
	ds_bpermute_b32 v5, v200, v2
	v_mov_b32_e32 v100, v133
	v_mov_b32_e32 v101, v133
	v_and_b32_e32 v203, 48, v0
	v_mov_b32_e32 v98, v133
	s_waitcnt lgkmcnt(0)
	v_add_f32_e32 v2, v2, v5
	v_xor_b32_e32 v5, 16, v3
	v_cmp_lt_i32_e32 vcc, v5, v4
	v_mov_b32_e32 v99, v133
	v_mov_b64_e32 v[104:105], v[100:101]
	v_cndmask_b32_e32 v5, v3, v5, vcc
	v_lshlrev_b32_e32 v201, 2, v5
	ds_bpermute_b32 v5, v201, v2
	v_mov_b64_e32 v[108:109], v[100:101]
	v_mov_b64_e32 v[112:113], v[100:101]
	v_mov_b64_e32 v[116:117], v[100:101]
	v_mov_b64_e32 v[120:121], v[100:101]
	s_waitcnt lgkmcnt(0)
	v_add_f32_e32 v2, v2, v5
	v_xor_b32_e32 v5, 8, v3
	v_cmp_lt_i32_e32 vcc, v5, v4
	v_mov_b64_e32 v[124:125], v[100:101]
	v_mov_b64_e32 v[128:129], v[100:101]
	v_cndmask_b32_e32 v5, v3, v5, vcc
	v_lshlrev_b32_e32 v205, 2, v5
	ds_bpermute_b32 v5, v205, v2
	v_cmp_eq_u32_e64 s[8:9], 0, v131
	v_mov_b32_e32 v218, 0xff800000
	v_mov_b32_e32 v213, 0x23420
	v_mov_b64_e32 v[102:103], v[98:99]
	s_waitcnt lgkmcnt(0)
	v_add_f32_e32 v2, v2, v5
	v_xor_b32_e32 v5, 4, v3
	v_cmp_lt_i32_e32 vcc, v5, v4
	v_mov_b64_e32 v[106:107], v[98:99]
	v_mov_b64_e32 v[110:111], v[98:99]
	v_cndmask_b32_e32 v5, v3, v5, vcc
	v_lshlrev_b32_e32 v206, 2, v5
	ds_bpermute_b32 v5, v206, v2
	v_mov_b64_e32 v[114:115], v[98:99]
	v_mov_b64_e32 v[118:119], v[98:99]
	v_mov_b64_e32 v[122:123], v[98:99]
	v_mov_b64_e32 v[126:127], v[98:99]
	s_waitcnt lgkmcnt(0)
	v_add_f32_e32 v2, v2, v5
	v_xor_b32_e32 v5, 2, v3
	v_cmp_lt_i32_e32 vcc, v5, v4
	v_mov_b32_e32 v219, 0
	s_mov_b32 s35, s31
	v_cndmask_b32_e32 v5, v3, v5, vcc
	v_lshlrev_b32_e32 v207, 2, v5
	ds_bpermute_b32 v5, v207, v2
	v_mov_b32_e32 v138, 0
	v_mov_b32_e32 v139, v133
	v_mov_b32_e32 v136, 0
	v_mov_b32_e32 v137, v133
	s_waitcnt lgkmcnt(0)
	v_add_f32_e32 v2, v2, v5
	v_xor_b32_e32 v5, 1, v3
	v_cmp_lt_i32_e32 vcc, v5, v4
	v_lshlrev_b32_e32 v4, 3, v131
	v_mov_b32_e32 v144, 0
	v_cndmask_b32_e32 v3, v3, v5, vcc
	v_lshlrev_b32_e32 v208, 2, v3
	ds_bpermute_b32 v3, v208, v2
	v_mov_b32_e32 v145, v133
	v_mov_b32_e32 v142, 0
	v_mov_b32_e32 v143, v133
	v_mov_b32_e32 v150, 0
	s_waitcnt lgkmcnt(0)
	v_add_f32_e32 v2, v2, v3
	v_add_f32_e32 v2, s43, v2
	s_mul_i32 s4, s31, 0x2200
	s_add_i32 s24, s4, 0x11000
	v_mul_f32_e32 v210, 0x3fb8aa3b, v2
	s_movk_i32 s4, 0x220
	v_mov_b32_e32 v2, s24
	v_mad_u32_u24 v5, v202, s4, v2
	v_lshlrev_b64 v[2:3], 9, v[132:133]
	v_lshl_add_u64 v[2:3], s[6:7], 0, v[2:3]
	v_lshlrev_b32_e32 v132, 5, v209
	v_add_u32_e32 v212, s24, v4
	v_mad_u32_u24 v211, v202, s4, v203
	v_lshl_add_u64 v[134:135], v[2:3], 0, v[132:133]
	v_cmp_eq_u32_e64 s[6:7], 15, v202
	v_cmp_eq_u32_e64 s[4:5], 15, v131
	v_add_u32_e32 v214, v5, v203
	v_add_u32_e32 v215, 0x800, v212
	v_add_u32_e32 v216, 0x1000, v212
	v_add_u32_e32 v217, 0x1800, v212
	v_mov_b32_e32 v151, v133
	v_mov_b32_e32 v140, 0
	v_mov_b32_e32 v141, v133
	v_mov_b32_e32 v148, 0
	v_mov_b32_e32 v149, v133
	v_mov_b32_e32 v146, 0
	v_mov_b32_e32 v147, v133
	v_mov_b32_e32 v178, 0
	v_mov_b32_e32 v179, v133
	v_mov_b32_e32 v168, 0
	v_mov_b32_e32 v169, v133
	v_mov_b32_e32 v154, 0
	v_mov_b32_e32 v155, v133
	v_mov_b32_e32 v152, 0
	v_mov_b32_e32 v153, v133
	v_mov_b32_e32 v182, 0
	v_mov_b32_e32 v183, v133
	v_mov_b32_e32 v180, 0
	v_mov_b32_e32 v181, v133
	v_mov_b32_e32 v158, 0
	v_mov_b32_e32 v159, v133
	v_mov_b32_e32 v156, 0
	v_mov_b32_e32 v157, v133
	v_mov_b32_e32 v186, 0
	v_mov_b32_e32 v187, v133
	v_mov_b32_e32 v184, 0
	v_mov_b32_e32 v185, v133
	v_mov_b32_e32 v162, 0
	v_mov_b32_e32 v163, v133
	v_mov_b32_e32 v160, 0
	v_mov_b32_e32 v161, v133
	v_mov_b32_e32 v190, 0
	v_mov_b32_e32 v191, v133
	v_mov_b32_e32 v188, 0
	v_mov_b32_e32 v189, v133
	v_mov_b32_e32 v166, 0
	v_mov_b32_e32 v167, v133
	v_mov_b32_e32 v164, 0
	v_mov_b32_e32 v165, v133
	v_mov_b32_e32 v194, 0
	v_mov_b32_e32 v195, v133
	v_mov_b32_e32 v192, 0
	v_mov_b32_e32 v193, v133
	v_mov_b32_e32 v172, 0
	v_mov_b32_e32 v173, v133
	v_mov_b32_e32 v170, 0
	v_mov_b32_e32 v171, v133
	v_mov_b32_e32 v198, 0
	v_mov_b32_e32 v199, v133
	v_mov_b32_e32 v196, 0
	v_mov_b32_e32 v197, v133
	v_mov_b32_e32 v176, 0
	v_mov_b32_e32 v177, v133
	v_mov_b32_e32 v174, 0
	v_mov_b32_e32 v175, v133
	s_cmp_eq_u32 s2, 0
	s_cselect_b64 s[24:25], -1, 0
	s_and_b64 s[24:25], s[24:25], s[10:11]
	s_and_saveexec_b64 s[26:27], s[24:25]
	s_cbranch_execz .Lp1_noinit
	global_store_dword v[254:255], v253, off
